# once a wave's staging stream is finished, the K/V piece wait returns to the step end (as in the baseline) instead of the 15th MFMA gap
# baseline (speedup 1.0000x reference)
.Lcs_done_h0:
	s_branch .Lcs_noL_h0

; __device__ __forceinline__ void convert_moe_items(const Ctx& a, int layer, LAS unsigned char* lds, int it0, int it1, int widx, int nw, int wave, int lane) {
;     ...
;     auto decode = [&](int it) { CvtItem d; const int e = it / PER_E; int r = it % PER_E; const size_t eo = ((size_t)layer * NE + e) * (size_t)DM * FE;
;         if (r < I_G)          { d.src = wg + eo; d.dst = WGU; d.N = FE; d.K = DM; d.row_off = e * 2048; d.ilv = 1; }
;         else if (r < 2 * I_G) { r -= I_G; d.src = wu + eo; d.dst = WGU; d.N = FE; d.K = DM; d.row_off = e * 2048 + 128; d.ilv = 1; }
;         else                  { r -= 2 * I_G; d.src = wd + eo; d.dst = WD; d.N = DM; d.K = FE; d.row_off = e * 2048; d.ilv = 0; }
;         const int nblk = d.N / 32; d.k0 = 64 * (r / nblk); d.n0 = 32 * (r % nblk); return d; };
.Lcs_down_h0:
	s_addk_i32 s79, 0xf800
	s_add_u32 s98, s72, s80
	s_addc_u32 s99, s73, 0
	s_lshr_b32 s82, s79, 6
	s_lshl_b32 s82, s82, 6
	s_and_b32 s83, s79, 63
	s_lshl_b32 s83, s83, 5
	s_lshl_b32 s84, s82, 13
	s_lshl_b32 s85, s83, 2
	s_add_i32 s84, s84, s85
	s_add_u32 s98, s98, s84
	s_addc_u32 s99, s99, 0
	s_mov_b32 s62, 0x10000
	s_mov_b32 s88, 0x4000
	s_mov_b32 s89, 0xbfc0
	s_add_i32 s84, s81, s83
	s_lshl_b32 s84, s84, 11
	s_lshl_b32 s85, s82, 1
	s_add_i32 s84, s84, s85
	s_add_u32 s64, s76, s84
	s_addc_u32 s65, s77, 0
	s_lshr_b32 s91, s91, 1
	s_sub_u32 s64, s64, s91
	s_subb_u32 s65, s65, 0
	v_mov_b32_e32 v25, v246
	v_lshrrev_b32_e32 v33, 1, v24
	s_branch .Lcs_Lgo_h0
.Lcs_doneW_h0:
	s_waitcnt vmcnt(4)
	s_branch .Lcs_noW_h0
.Lcs_R_h0:
	ds_read_b64 v[254:255], v32
	ds_read_b64 v[30:31], v32 offset:576
	ds_read_b64 v[22:23], v32 offset:1152
	ds_read_b64 v[26:27], v32 offset:1728
	s_branch .Lcs_W_h0

.Lcs_adopt_h1:
	s_mov_b64 s[100:101], s[64:65]
	v_mov_b32_e32 v28, v33
	s_mov_b32 s63, s88
	s_mov_b32 s87, s89
	s_branch .Lcs_Sgo_h1
.Lcs_doneW_h1:
	s_waitcnt vmcnt(4)
	s_branch .Lcs_noW_h1
.LBB0_542:
	v_mov_b32_e32 v18, 0
	v_mov_b32_e32 v19, 0
	v_mov_b32_e32 v20, 0
	v_mov_b32_e32 v21, 0
	v_mov_b32_e32 v22, 0
	v_mov_b32_e32 v23, 0
	v_mov_b32_e32 v24, 0
	v_mov_b32_e32 v25, 0
	v_mov_b32_e32 v26, 0
	v_mov_b32_e32 v27, 0
	v_mov_b32_e32 v28, 0
	v_mov_b32_e32 v29, 0
	v_mov_b32_e32 v30, 0
	v_mov_b32_e32 v31, 0
	v_mov_b32_e32 v32, 0
	v_mov_b32_e32 v33, 0
	s_mov_b32 m0, s32
	ds_read_b128 v[240:243], v233
	v_add_f32_e32 v3, v130, v131
	v_add_f32_e32 v3, v132, v3
	v_add_f32_e32 v3, v133, v3
	v_add_f32_e32 v3, v134, v3
	s_waitcnt lgkmcnt(0)
	v_mfma_f32_32x32x16_bf16 v[162:177], v[146:149], v[240:243], v[98:113]
	v_add_f32_e32 v3, v135, v3
	v_cvt_pk_bf16_f32 v194, v130, v131
	v_cvt_pk_bf16_f32 v195, v132, v133
	v_mfma_f32_32x32x16_bf16 v[146:161], v[202:205], v[240:243], v[98:113]
	v_add_f32_e32 v3, v136, v3
	v_add_f32_e32 v3, v137, v3
	v_add_f32_e32 v3, v138, v3
	v_add_f32_e32 v3, v139, v3
	v_cvt_pk_bf16_f32 v196, v134, v135
	v_cvt_pk_bf16_f32 v197, v136, v137
	ds_read_b128 v[130:133], v233 offset:1024
	v_add_f32_e32 v3, v140, v3
	v_add_f32_e32 v3, v141, v3
	v_add_f32_e32 v3, v142, v3
	v_add_f32_e32 v3, v143, v3
	s_waitcnt lgkmcnt(0)
	v_mfma_f32_32x32x16_bf16 v[162:177], v[206:209], v[130:133], v[162:177]
	v_cvt_pk_bf16_f32 v12, v138, v139
	v_cvt_pk_bf16_f32 v13, v140, v141
	v_mfma_f32_32x32x16_bf16 v[146:161], v[190:193], v[130:133], v[146:161]
	v_add_f32_e32 v3, v144, v3
	v_add_f32_e32 v3, v145, v3
	v_add_f32_e32 v3, v114, v3
	v_add_f32_e32 v3, v115, v3
	v_cvt_pk_bf16_f32 v14, v142, v143
	v_cvt_pk_bf16_f32 v15, v144, v145
	ds_read_b128 v[138:141], v233 offset:2048
	ds_read_b64_tr_b16 v[134:135], v223 offset:49152
	ds_read_b64_tr_b16 v[136:137], v223 offset:49664
	s_waitcnt lgkmcnt(2)
	v_mfma_f32_32x32x16_bf16 v[162:177], v[198:201], v[138:141], v[162:177]
	v_add_f32_e32 v3, v116, v3
	v_add_f32_e32 v3, v117, v3
	v_add_f32_e32 v3, v118, v3
	v_add_f32_e32 v3, v119, v3
	v_cvt_pk_bf16_f32 v8, v114, v115
	v_cvt_pk_bf16_f32 v9, v116, v117
	ds_read_b64_tr_b16 v[130:131], v223 offset:53248
	ds_read_b64_tr_b16 v[132:133], v223 offset:53760
	v_mfma_f32_32x32x16_bf16 v[146:161], v[186:189], v[138:141], v[146:161]
	v_add_f32_e32 v3, v120, v3
	v_add_f32_e32 v3, v121, v3
	v_add_f32_e32 v3, v122, v3
	v_add_f32_e32 v3, v123, v3
	v_cvt_pk_bf16_f32 v10, v118, v119
	v_cvt_pk_bf16_f32 v11, v120, v121
	ds_read_b128 v[138:141], v233 offset:3072
	ds_read_b64_tr_b16 v[118:119], v223 offset:57344
	ds_read_b64_tr_b16 v[120:121], v223 offset:57856
	s_waitcnt lgkmcnt(2)
	v_mfma_f32_32x32x16_bf16 v[162:177], v[182:185], v[138:141], v[162:177]
	v_add_f32_e32 v3, v124, v3
	v_add_f32_e32 v3, v125, v3
	v_add_f32_e32 v3, v126, v3
	v_add_f32_e32 v3, v127, v3
	v_cvt_pk_bf16_f32 v4, v122, v123
	v_cvt_pk_bf16_f32 v5, v124, v125
	ds_read_b64_tr_b16 v[114:115], v223 offset:61440
	ds_read_b64_tr_b16 v[116:117], v223 offset:61952
	v_mfma_f32_32x32x16_bf16 v[146:161], v[178:181], v[138:141], v[146:161]
	v_add_f32_e32 v3, v128, v3
	v_add_f32_e32 v3, v129, v3
	v_add_f32_e32 v3, 0, v3
	v_cvt_pk_bf16_f32 v6, v126, v127
	v_cvt_pk_bf16_f32 v7, v128, v129
	v_max_f32_e32 v16, v163, v163
	v_max_f32_e32 v17, v162, v162
	v_max_f32_e32 v16, v17, v16
	s_nop 3
	v_max3_f32 v17, v164, v165, v147
	v_max3_f32 v16, v16, v146, v148
	v_max3_f32 v16, v16, v149, v166
	v_max3_f32 v17, v17, v168, v169
	v_max3_f32 v16, v16, v167, v150
	v_max3_f32 v17, v17, v152, v153
	v_max3_f32 v16, v16, v151, v170
	v_max3_f32 v17, v17, v172, v173
	v_max3_f32 v16, v16, v171, v154
	v_max3_f32 v17, v17, v156, v157
	v_max3_f32 v16, v16, v155, v174
	v_max3_f32 v17, v17, v176, v177
	v_max3_f32 v122, v16, v175, v158
	v_max3_f32 v17, v17, v160, v161
	v_add_f32_e32 v16, v238, v3
	v_max3_f32 v3, v122, v159, v17
	v_mov_b32_e32 v17, v3
	s_nop 1
	v_permlane32_swap_b32_e32 v3, v17
	v_max_f32_e32 v17, v17, v17
	v_max_f32_e32 v3, v3, v3
	v_max_f32_e32 v3, v3, v17
	v_cmp_lt_f32_e32 vcc, s30, v3
	s_cmp_lg_u64 vcc, 0
	s_cselect_b64 s[0:1], -1, 0
	s_cbranch_vccnz .LBB0_565
